# hand-written 128x128 wconv with write-through stores; sc1 stores in LN and retention kernels; nt loads of fp16 residual and partials in LN; 4-phase GEMM loops
# speedup vs baseline: 1.0277x; 1.0053x over previous
.Lwc_work:
	s_load_dword s8, s[0:1], 0x150
	s_cmp_eq_u32 s3, 5
	s_cselect_b32 s9, 13, 11
	s_cmp_eq_u32 s3, 6
	s_cselect_b32 s10, 13, 11
	s_sub_u32 s11, s9, 7
	s_lshr_b32 s12, s4, s11
	s_lshl_b32 s13, s12, s11
	s_sub_u32 s13, s4, s13
	s_add_u32 s20, s9, 2
	s_add_u32 s21, s10, 1
	v_lshrrev_b32_e32 v4, 5, v0
	v_and_b32_e32 v6, 31, v0
	v_lshlrev_b32_e32 v5, 4, v4
	v_lshlrev_b32_e32 v5, s20, v5
	v_lshl_add_u32 v1, v6, 4, v5
	v_lshlrev_b32_e32 v7, 1, v4
	v_and_b32_e32 v8, 7, v6
	v_xor_b32_e32 v7, v7, v8
	v_lshlrev_b32_e32 v7, 4, v7
	v_lshl_add_u32 v2, v6, 10, v7
	v_xor_b32_e32 v3, 16, v2
	v_lshrrev_b32_e32 v9, 4, v0
	v_and_b32_e32 v10, 15, v0
	v_lshrrev_b32_e32 v11, 6, v0
	v_xor_b32_e32 v11, v10, v11
	v_lshlrev_b32_e32 v11, 4, v11
	v_lshl_add_u32 v100, v9, 8, v11
	v_xor_b32_e32 v101, 64, v100
	v_lshlrev_b32_e32 v12, s21, v9
	v_lshl_add_u32 v102, v10, 4, v12
	s_add_u32 s22, s20, 7
	s_lshl_b32 s23, s12, s22
	s_lshl_b32 s24, s13, 9
	s_add_u32 s23, s23, s24
	s_lshl_b32 s25, 1, s20
	s_add_u32 s26, s21, 7
	s_lshl_b32 s27, s13, s26
	s_lshl_b32 s28, s12, 8
	s_add_u32 s27, s27, s28
	s_add_u32 s29, s10, 5
	s_lshl_b32 s29, 1, s29
	s_waitcnt lgkmcnt(0)
	s_add_u32 s8, s8, s3
	s_lshl_b32 s8, s8, 3
	s_add_u32 s14, s0, s8
	s_addc_u32 s15, s1, 0
	s_load_dwordx2 s[16:17], s[14:15], 0x0
	s_load_dwordx2 s[18:19], s[14:15], 0x70
	s_waitcnt lgkmcnt(0)
	s_add_u32 s16, s16, s23
	s_addc_u32 s17, s17, 0
	s_add_u32 s18, s18, s27
	s_addc_u32 s19, s19, 0
	global_load_dwordx4 v[4:7], v1, s[16:17] nt
	s_add_u32 s16, s16, s25
	s_addc_u32 s17, s17, 0
	global_load_dwordx4 v[8:11], v1, s[16:17] nt
	s_add_u32 s16, s16, s25
	s_addc_u32 s17, s17, 0
	global_load_dwordx4 v[12:15], v1, s[16:17] nt
	s_add_u32 s16, s16, s25
	s_addc_u32 s17, s17, 0
	global_load_dwordx4 v[16:19], v1, s[16:17] nt
	s_add_u32 s16, s16, s25
	s_addc_u32 s17, s17, 0
	global_load_dwordx4 v[20:23], v1, s[16:17] nt
	s_add_u32 s16, s16, s25
	s_addc_u32 s17, s17, 0
	global_load_dwordx4 v[24:27], v1, s[16:17] nt
	s_add_u32 s16, s16, s25
	s_addc_u32 s17, s17, 0
	global_load_dwordx4 v[28:31], v1, s[16:17] nt
	s_add_u32 s16, s16, s25
	s_addc_u32 s17, s17, 0
	global_load_dwordx4 v[32:35], v1, s[16:17] nt
	s_add_u32 s16, s16, s25
	s_addc_u32 s17, s17, 0
	global_load_dwordx4 v[36:39], v1, s[16:17] nt
	s_add_u32 s16, s16, s25
	s_addc_u32 s17, s17, 0
	global_load_dwordx4 v[40:43], v1, s[16:17] nt
	s_add_u32 s16, s16, s25
	s_addc_u32 s17, s17, 0
	global_load_dwordx4 v[44:47], v1, s[16:17] nt
	s_add_u32 s16, s16, s25
	s_addc_u32 s17, s17, 0
	global_load_dwordx4 v[48:51], v1, s[16:17] nt
	s_add_u32 s16, s16, s25
	s_addc_u32 s17, s17, 0
	global_load_dwordx4 v[52:55], v1, s[16:17] nt
	s_add_u32 s16, s16, s25
	s_addc_u32 s17, s17, 0
	global_load_dwordx4 v[56:59], v1, s[16:17] nt
	s_add_u32 s16, s16, s25
	s_addc_u32 s17, s17, 0
	global_load_dwordx4 v[60:63], v1, s[16:17] nt
	s_add_u32 s16, s16, s25
	s_addc_u32 s17, s17, 0
	global_load_dwordx4 v[64:67], v1, s[16:17] nt
	s_waitcnt vmcnt(14)
	v_cvt_pk_f16_f32 v68, v4, v8
	v_cvt_pk_f16_f32 v76, v5, v9
	v_cvt_pk_f16_f32 v84, v6, v10
	v_cvt_pk_f16_f32 v92, v7, v11
	s_waitcnt vmcnt(12)
	v_cvt_pk_f16_f32 v69, v12, v16
	v_cvt_pk_f16_f32 v77, v13, v17
	v_cvt_pk_f16_f32 v85, v14, v18
	v_cvt_pk_f16_f32 v93, v15, v19
	s_waitcnt vmcnt(10)
	v_cvt_pk_f16_f32 v70, v20, v24
	v_cvt_pk_f16_f32 v78, v21, v25
	v_cvt_pk_f16_f32 v86, v22, v26
	v_cvt_pk_f16_f32 v94, v23, v27
	s_waitcnt vmcnt(8)
	v_cvt_pk_f16_f32 v71, v28, v32
	v_cvt_pk_f16_f32 v79, v29, v33
	v_cvt_pk_f16_f32 v87, v30, v34
	v_cvt_pk_f16_f32 v95, v31, v35
	ds_write_b128 v2, v[68:71]
	ds_write_b128 v2, v[76:79] offset:256
	ds_write_b128 v2, v[84:87] offset:512
	ds_write_b128 v2, v[92:95] offset:768
	s_waitcnt vmcnt(6)
	v_cvt_pk_f16_f32 v72, v36, v40
	v_cvt_pk_f16_f32 v80, v37, v41
	v_cvt_pk_f16_f32 v88, v38, v42
	v_cvt_pk_f16_f32 v96, v39, v43
	s_waitcnt vmcnt(4)
	v_cvt_pk_f16_f32 v73, v44, v48
	v_cvt_pk_f16_f32 v81, v45, v49
	v_cvt_pk_f16_f32 v89, v46, v50
	v_cvt_pk_f16_f32 v97, v47, v51
	s_waitcnt vmcnt(2)
	v_cvt_pk_f16_f32 v74, v52, v56
	v_cvt_pk_f16_f32 v82, v53, v57
	v_cvt_pk_f16_f32 v90, v54, v58
	v_cvt_pk_f16_f32 v98, v55, v59
	s_waitcnt vmcnt(0)
	v_cvt_pk_f16_f32 v75, v60, v64
	v_cvt_pk_f16_f32 v83, v61, v65
	v_cvt_pk_f16_f32 v91, v62, v66
	v_cvt_pk_f16_f32 v99, v63, v67
	ds_write_b128 v3, v[72:75]
	ds_write_b128 v3, v[80:83] offset:256
	ds_write_b128 v3, v[88:91] offset:512
	ds_write_b128 v3, v[96:99] offset:768
	s_waitcnt lgkmcnt(0)
	s_barrier
	ds_read_b128 v[4:7], v100
	ds_read_b128 v[8:11], v101 offset:4096
	ds_read_b128 v[12:15], v100 offset:8192
	ds_read_b128 v[16:19], v101 offset:12288
	ds_read_b128 v[20:23], v100 offset:16384
	ds_read_b128 v[24:27], v101 offset:20480
	ds_read_b128 v[28:31], v100 offset:24576
	ds_read_b128 v[32:35], v101 offset:28672
	s_waitcnt lgkmcnt(7)
	global_store_dwordx4 v102, v[4:7], s[18:19] sc1
	s_add_u32 s18, s18, s29
	s_addc_u32 s19, s19, 0
	s_waitcnt lgkmcnt(6)
	global_store_dwordx4 v102, v[8:11], s[18:19] sc1
	s_add_u32 s18, s18, s29
	s_addc_u32 s19, s19, 0
	s_waitcnt lgkmcnt(5)
	global_store_dwordx4 v102, v[12:15], s[18:19] sc1
	s_add_u32 s18, s18, s29
	s_addc_u32 s19, s19, 0
	s_waitcnt lgkmcnt(4)
	global_store_dwordx4 v102, v[16:19], s[18:19] sc1
	s_add_u32 s18, s18, s29
	s_addc_u32 s19, s19, 0
	s_waitcnt lgkmcnt(3)
	global_store_dwordx4 v102, v[20:23], s[18:19] sc1
	s_add_u32 s18, s18, s29
	s_addc_u32 s19, s19, 0
	s_waitcnt lgkmcnt(2)
	global_store_dwordx4 v102, v[24:27], s[18:19] sc1
	s_add_u32 s18, s18, s29
	s_addc_u32 s19, s19, 0
	s_waitcnt lgkmcnt(1)
	global_store_dwordx4 v102, v[28:31], s[18:19] sc1
	s_add_u32 s18, s18, s29
	s_addc_u32 s19, s19, 0
	s_waitcnt lgkmcnt(0)
	global_store_dwordx4 v102, v[32:35], s[18:19] sc1

_Z9ln_kernelILb0ELb0EEvPKvPKtS3_PKfPvPtS5_S5_:
	s_load_dwordx8 s[4:11], s[0:1], 0x0
	s_ashr_i32 s3, s2, 31
	v_lshlrev_b32_e32 v18, 2, v0
	s_lshl_b64 s[14:15], s[2:3], 11
	v_or_b32_e32 v6, s14, v18
	v_mov_b32_e32 v7, s15
	s_waitcnt lgkmcnt(0)
	v_lshl_add_u64 v[2:3], v[6:7], 2, s[4:5]
	global_load_dwordx4 v[2:5], v[2:3], off nt
	s_cmp_lg_u64 s[6:7], 0
	s_cselect_b64 s[18:19], -1, 0
	s_and_b64 vcc, exec, s[18:19]
	v_lshlrev_b64 v[12:13], 1, v[6:7]
	s_cbranch_vccz .LBB2_2
	v_lshl_add_u64 v[8:9], s[6:7], 0, v[12:13]
	v_lshl_add_u64 v[10:11], s[8:9], 0, v[12:13]
	global_load_dwordx2 v[8:9], v[8:9], off nt
	s_waitcnt vmcnt(0)
	v_cvt_f32_f16_e32 v14, v8
	global_load_dwordx2 v[10:11], v[10:11], off nt
	v_cvt_f32_f16_sdwa v15, v8 dst_sel:DWORD dst_unused:UNUSED_PAD src0_sel:WORD_1
	v_cvt_f32_f16_e32 v8, v9
	v_cvt_f32_f16_sdwa v9, v9 dst_sel:DWORD dst_unused:UNUSED_PAD src0_sel:WORD_1
	s_waitcnt vmcnt(0)
	v_cvt_f32_f16_e32 v16, v10
	v_cvt_f32_f16_sdwa v17, v10 dst_sel:DWORD dst_unused:UNUSED_PAD src0_sel:WORD_1
	v_cvt_f32_f16_e32 v10, v11
	v_cvt_f32_f16_sdwa v11, v11 dst_sel:DWORD dst_unused:UNUSED_PAD src0_sel:WORD_1
	v_pk_add_f32 v[14:15], v[14:15], v[16:17]
	s_nop 0
	v_pk_add_f32 v[2:3], v[14:15], v[2:3]
	v_pk_add_f32 v[8:9], v[8:9], v[10:11]
	s_nop 0
	v_pk_add_f32 v[4:5], v[8:9], v[4:5]

.LBB2_6:
	v_or_b32_e32 v16, 0x400, v18
	v_mov_b32_e32 v17, 0
	v_lshl_add_u64 v[14:15], s[14:15], 0, v[16:17]
	v_lshl_add_u64 v[6:7], v[14:15], 2, s[4:5]
	global_load_dwordx4 v[6:9], v[6:7], off nt
	s_andn2_b64 vcc, exec, s[18:19]
	s_cbranch_vccnz .LBB2_8
	v_lshl_add_u64 v[20:21], s[6:7], 0, v[12:13]
	v_lshl_add_u64 v[12:13], s[8:9], 0, v[12:13]
	global_load_dwordx2 v[20:21], v[20:21], off offset:2048 nt
	s_waitcnt vmcnt(0)
	v_cvt_f32_f16_e32 v22, v20
	global_load_dwordx2 v[12:13], v[12:13], off offset:2048 nt
	v_cvt_f32_f16_sdwa v23, v20 dst_sel:DWORD dst_unused:UNUSED_PAD src0_sel:WORD_1
	v_cvt_f32_f16_e32 v20, v21
	v_cvt_f32_f16_sdwa v21, v21 dst_sel:DWORD dst_unused:UNUSED_PAD src0_sel:WORD_1
	s_waitcnt vmcnt(0)
	v_cvt_f32_f16_e32 v24, v12
	v_cvt_f32_f16_sdwa v25, v12 dst_sel:DWORD dst_unused:UNUSED_PAD src0_sel:WORD_1
	v_cvt_f32_f16_e32 v12, v13
	v_cvt_f32_f16_sdwa v13, v13 dst_sel:DWORD dst_unused:UNUSED_PAD src0_sel:WORD_1
	v_pk_add_f32 v[22:23], v[22:23], v[24:25]
	s_nop 0
	v_pk_add_f32 v[6:7], v[22:23], v[6:7]
	v_pk_add_f32 v[12:13], v[20:21], v[12:13]
	s_nop 0
	v_pk_add_f32 v[8:9], v[12:13], v[8:9]

_Z9ln_kernelILb1ELb1EEvPKvPKtS3_PKfPvPtS5_S5_:
	s_load_dwordx8 s[4:11], s[0:1], 0x0
	s_ashr_i32 s3, s2, 31
	v_lshlrev_b32_e32 v26, 2, v0
	s_lshl_b64 s[12:13], s[2:3], 11
	v_or_b32_e32 v14, s12, v26
	v_mov_b32_e32 v15, s13
	s_waitcnt lgkmcnt(0)
	v_lshl_add_u64 v[12:13], v[14:15], 1, s[4:5]
	global_load_dwordx2 v[4:5], v[12:13], off nt
	s_cmp_lg_u64 s[6:7], 0
	s_cselect_b64 s[12:13], -1, 0
	s_and_b64 vcc, exec, s[12:13]
	v_lshlrev_b64 v[10:11], 1, v[14:15]
	s_waitcnt vmcnt(0)
	v_cvt_f32_f16_e32 v2, v4
	v_cvt_f32_f16_sdwa v3, v4 dst_sel:DWORD dst_unused:UNUSED_PAD src0_sel:WORD_1
	v_cvt_f32_f16_e32 v4, v5
	v_cvt_f32_f16_sdwa v5, v5 dst_sel:DWORD dst_unused:UNUSED_PAD src0_sel:WORD_1
	s_cbranch_vccz .LBB3_2
	v_lshl_add_u64 v[6:7], s[6:7], 0, v[10:11]
	v_lshl_add_u64 v[8:9], s[8:9], 0, v[10:11]
	global_load_dwordx2 v[6:7], v[6:7], off nt
	s_waitcnt vmcnt(0)
	v_cvt_f32_f16_e32 v16, v6
	global_load_dwordx2 v[8:9], v[8:9], off nt
	v_cvt_f32_f16_sdwa v17, v6 dst_sel:DWORD dst_unused:UNUSED_PAD src0_sel:WORD_1
	v_cvt_f32_f16_e32 v6, v7
	v_cvt_f32_f16_sdwa v7, v7 dst_sel:DWORD dst_unused:UNUSED_PAD src0_sel:WORD_1
	s_waitcnt vmcnt(0)
	v_cvt_f32_f16_e32 v18, v8
	v_cvt_f32_f16_sdwa v19, v8 dst_sel:DWORD dst_unused:UNUSED_PAD src0_sel:WORD_1
	v_cvt_f32_f16_e32 v8, v9
	v_cvt_f32_f16_sdwa v9, v9 dst_sel:DWORD dst_unused:UNUSED_PAD src0_sel:WORD_1
	v_pk_add_f32 v[16:17], v[16:17], v[18:19]
	s_nop 0
	v_pk_add_f32 v[2:3], v[16:17], v[2:3]
	v_pk_add_f32 v[6:7], v[6:7], v[8:9]
	s_nop 0
	v_pk_add_f32 v[4:5], v[6:7], v[4:5]

.LBB3_6:
	global_load_dwordx2 v[12:13], v[12:13], off offset:2048 nt
	s_andn2_b64 vcc, exec, s[12:13]
	s_waitcnt vmcnt(0)
	v_cvt_f32_f16_sdwa v25, v12 dst_sel:DWORD dst_unused:UNUSED_PAD src0_sel:WORD_1
	v_cvt_f32_f16_e32 v24, v12
	v_cvt_f32_f16_sdwa v23, v13 dst_sel:DWORD dst_unused:UNUSED_PAD src0_sel:WORD_1
	v_cvt_f32_f16_e32 v22, v13
	s_cbranch_vccnz .LBB3_8
	v_lshl_add_u64 v[12:13], s[6:7], 0, v[10:11]
	v_lshl_add_u64 v[10:11], s[8:9], 0, v[10:11]
	global_load_dwordx2 v[12:13], v[12:13], off offset:2048 nt
	s_waitcnt vmcnt(0)
	v_cvt_f32_f16_e32 v14, v12
	global_load_dwordx2 v[10:11], v[10:11], off offset:2048 nt
	v_cvt_f32_f16_sdwa v15, v12 dst_sel:DWORD dst_unused:UNUSED_PAD src0_sel:WORD_1
	v_cvt_f32_f16_e32 v12, v13
	v_cvt_f32_f16_sdwa v13, v13 dst_sel:DWORD dst_unused:UNUSED_PAD src0_sel:WORD_1
	s_waitcnt vmcnt(0)
	v_cvt_f32_f16_e32 v16, v10
	v_cvt_f32_f16_sdwa v17, v10 dst_sel:DWORD dst_unused:UNUSED_PAD src0_sel:WORD_1
	v_cvt_f32_f16_e32 v10, v11
	v_cvt_f32_f16_sdwa v11, v11 dst_sel:DWORD dst_unused:UNUSED_PAD src0_sel:WORD_1
	v_pk_add_f32 v[14:15], v[14:15], v[16:17]
	s_nop 0
	v_pk_add_f32 v[24:25], v[14:15], v[24:25]
	v_pk_add_f32 v[10:11], v[12:13], v[10:11]
	s_nop 0
	v_pk_add_f32 v[22:23], v[10:11], v[22:23]

_Z9ln_kernelILb0ELb1EEvPKvPKtS3_PKfPvPtS5_S5_:
	s_load_dwordx8 s[4:11], s[0:1], 0x0
	s_ashr_i32 s3, s2, 31
	v_lshlrev_b32_e32 v28, 2, v0
	s_lshl_b64 s[12:13], s[2:3], 11
	v_or_b32_e32 v12, s12, v28
	v_mov_b32_e32 v13, s13
	s_waitcnt lgkmcnt(0)
	v_lshl_add_u64 v[2:3], v[12:13], 2, s[4:5]
	global_load_dwordx4 v[2:5], v[2:3], off nt
	s_cmp_lg_u64 s[6:7], 0
	s_cselect_b64 s[16:17], -1, 0
	s_and_b64 vcc, exec, s[16:17]
	v_lshlrev_b64 v[10:11], 1, v[12:13]
	s_cbranch_vccz .LBB6_2
	v_lshl_add_u64 v[6:7], s[6:7], 0, v[10:11]
	v_lshl_add_u64 v[8:9], s[8:9], 0, v[10:11]
	global_load_dwordx2 v[6:7], v[6:7], off nt
	s_waitcnt vmcnt(0)
	v_cvt_f32_f16_e32 v14, v6
	global_load_dwordx2 v[8:9], v[8:9], off nt
	v_cvt_f32_f16_sdwa v15, v6 dst_sel:DWORD dst_unused:UNUSED_PAD src0_sel:WORD_1
	v_cvt_f32_f16_e32 v6, v7
	v_cvt_f32_f16_sdwa v7, v7 dst_sel:DWORD dst_unused:UNUSED_PAD src0_sel:WORD_1
	s_waitcnt vmcnt(0)
	v_cvt_f32_f16_e32 v16, v8
	v_cvt_f32_f16_sdwa v17, v8 dst_sel:DWORD dst_unused:UNUSED_PAD src0_sel:WORD_1
	v_cvt_f32_f16_e32 v8, v9
	v_cvt_f32_f16_sdwa v9, v9 dst_sel:DWORD dst_unused:UNUSED_PAD src0_sel:WORD_1
	v_pk_add_f32 v[14:15], v[14:15], v[16:17]
	s_nop 0
	v_pk_add_f32 v[2:3], v[14:15], v[2:3]
	v_pk_add_f32 v[6:7], v[6:7], v[8:9]
	s_nop 0
	v_pk_add_f32 v[4:5], v[6:7], v[4:5]

.LBB6_6:
	v_or_b32_e32 v26, 0x400, v28
	v_mov_b32_e32 v27, 0
	v_lshl_add_u64 v[12:13], s[12:13], 0, v[26:27]
	v_lshl_add_u64 v[12:13], v[12:13], 2, s[4:5]
	global_load_dwordx4 v[18:21], v[12:13], off nt
	s_andn2_b64 vcc, exec, s[16:17]
	s_cbranch_vccnz .LBB6_8
	v_lshl_add_u64 v[12:13], s[6:7], 0, v[10:11]
	v_lshl_add_u64 v[10:11], s[8:9], 0, v[10:11]
	global_load_dwordx2 v[12:13], v[12:13], off offset:2048 nt
	s_waitcnt vmcnt(0)
	v_cvt_f32_f16_e32 v14, v12
	global_load_dwordx2 v[10:11], v[10:11], off offset:2048 nt
	v_cvt_f32_f16_sdwa v15, v12 dst_sel:DWORD dst_unused:UNUSED_PAD src0_sel:WORD_1
	v_cvt_f32_f16_e32 v12, v13
	v_cvt_f32_f16_sdwa v13, v13 dst_sel:DWORD dst_unused:UNUSED_PAD src0_sel:WORD_1
	s_waitcnt vmcnt(0)
	v_cvt_f32_f16_e32 v16, v10
	v_cvt_f32_f16_sdwa v17, v10 dst_sel:DWORD dst_unused:UNUSED_PAD src0_sel:WORD_1
	v_cvt_f32_f16_e32 v10, v11
	v_cvt_f32_f16_sdwa v11, v11 dst_sel:DWORD dst_unused:UNUSED_PAD src0_sel:WORD_1
	v_pk_add_f32 v[14:15], v[14:15], v[16:17]
	s_nop 0
	v_pk_add_f32 v[18:19], v[14:15], v[18:19]
	v_pk_add_f32 v[10:11], v[12:13], v[10:11]
	s_nop 0
	v_pk_add_f32 v[20:21], v[10:11], v[20:21]

_Z9ln_kernelILb1ELb0EEvPKvPKtS3_PKfPvPtS5_S5_:
	s_load_dwordx8 s[4:11], s[0:1], 0x0
	s_ashr_i32 s3, s2, 31
	v_lshlrev_b32_e32 v14, 2, v0
	s_lshl_b64 s[12:13], s[2:3], 11
	v_or_b32_e32 v8, s12, v14
	v_mov_b32_e32 v9, s13
	s_waitcnt lgkmcnt(0)
	v_lshl_add_u64 v[6:7], v[8:9], 1, s[4:5]
	global_load_dwordx2 v[4:5], v[6:7], off nt
	s_cmp_lg_u64 s[6:7], 0
	s_cselect_b64 s[16:17], -1, 0
	s_and_b64 vcc, exec, s[16:17]
	v_lshlrev_b64 v[12:13], 1, v[8:9]
	s_waitcnt vmcnt(0)
	v_cvt_f32_f16_e32 v2, v4
	v_cvt_f32_f16_sdwa v3, v4 dst_sel:DWORD dst_unused:UNUSED_PAD src0_sel:WORD_1
	v_cvt_f32_f16_e32 v4, v5
	v_cvt_f32_f16_sdwa v5, v5 dst_sel:DWORD dst_unused:UNUSED_PAD src0_sel:WORD_1
	s_cbranch_vccz .LBB8_2
	v_lshl_add_u64 v[10:11], s[6:7], 0, v[12:13]
	v_lshl_add_u64 v[16:17], s[8:9], 0, v[12:13]
	global_load_dwordx2 v[10:11], v[10:11], off nt
	s_waitcnt vmcnt(0)
	v_cvt_f32_f16_e32 v18, v10
	global_load_dwordx2 v[16:17], v[16:17], off nt
	v_cvt_f32_f16_sdwa v19, v10 dst_sel:DWORD dst_unused:UNUSED_PAD src0_sel:WORD_1
	v_cvt_f32_f16_e32 v10, v11
	v_cvt_f32_f16_sdwa v11, v11 dst_sel:DWORD dst_unused:UNUSED_PAD src0_sel:WORD_1
	s_waitcnt vmcnt(0)
	v_cvt_f32_f16_e32 v20, v16
	v_cvt_f32_f16_sdwa v21, v16 dst_sel:DWORD dst_unused:UNUSED_PAD src0_sel:WORD_1
	v_cvt_f32_f16_e32 v16, v17
	v_cvt_f32_f16_sdwa v17, v17 dst_sel:DWORD dst_unused:UNUSED_PAD src0_sel:WORD_1
	v_pk_add_f32 v[18:19], v[18:19], v[20:21]
	s_nop 0
	v_pk_add_f32 v[2:3], v[18:19], v[2:3]
	v_pk_add_f32 v[10:11], v[10:11], v[16:17]
	s_nop 0
	v_pk_add_f32 v[4:5], v[10:11], v[4:5]

.LBB8_6:
	global_load_dwordx2 v[16:17], v[6:7], off offset:2048 nt
	s_andn2_b64 vcc, exec, s[16:17]
	s_waitcnt vmcnt(0)
	v_cvt_f32_f16_sdwa v7, v16 dst_sel:DWORD dst_unused:UNUSED_PAD src0_sel:WORD_1
	v_cvt_f32_f16_e32 v6, v16
	v_cvt_f32_f16_sdwa v9, v17 dst_sel:DWORD dst_unused:UNUSED_PAD src0_sel:WORD_1
	v_cvt_f32_f16_e32 v8, v17
	s_cbranch_vccnz .LBB8_8
	v_lshl_add_u64 v[16:17], s[6:7], 0, v[12:13]
	v_lshl_add_u64 v[12:13], s[8:9], 0, v[12:13]
	global_load_dwordx2 v[16:17], v[16:17], off offset:2048 nt
	s_waitcnt vmcnt(0)
	v_cvt_f32_f16_e32 v18, v16
	global_load_dwordx2 v[12:13], v[12:13], off offset:2048 nt
	v_cvt_f32_f16_sdwa v19, v16 dst_sel:DWORD dst_unused:UNUSED_PAD src0_sel:WORD_1
	v_cvt_f32_f16_e32 v16, v17
	v_cvt_f32_f16_sdwa v17, v17 dst_sel:DWORD dst_unused:UNUSED_PAD src0_sel:WORD_1
	s_waitcnt vmcnt(0)
	v_cvt_f32_f16_e32 v20, v12
	v_cvt_f32_f16_sdwa v21, v12 dst_sel:DWORD dst_unused:UNUSED_PAD src0_sel:WORD_1
	v_cvt_f32_f16_e32 v12, v13
	v_cvt_f32_f16_sdwa v13, v13 dst_sel:DWORD dst_unused:UNUSED_PAD src0_sel:WORD_1
	v_pk_add_f32 v[18:19], v[18:19], v[20:21]
	s_nop 0
	v_pk_add_f32 v[6:7], v[18:19], v[6:7]
	v_pk_add_f32 v[12:13], v[16:17], v[12:13]
	s_nop 0
	v_pk_add_f32 v[8:9], v[12:13], v[8:9]
